# v82: M3 retention decay weights in separable form (per-lane chained 2^(lg*(a-8J)) x wave-uniform 2^(-lg*m) table, min of fwd/bwd products; no per-element exp)
# baseline (speedup 1.0000x reference)
.LBB0_555:
	s_and_b32 s33, s3, 1
	s_lshl_b32 s4, s33, 1
	s_add_i32 s14, s4, s18
	s_mul_i32 s4, s10, 0x1100
	s_lshl_b32 s5, s11, 7
	s_add_i32 s45, s4, s5
	s_lshl_b32 s22, s14, 6
	v_or_b32_e32 v2, s45, v116
	v_mov_b64_e32 v[50:51], s[88:89]
	s_mul_i32 s5, s14, 0x44
	s_ashr_i32 s23, s22, 31
	v_mad_i64_i32 v[2:3], s[14:15], v2, s60, v[50:51]
	s_lshl_b64 s[14:15], s[22:23], 1
	v_mov_b32_e32 v101, v0
	v_lshl_add_u64 v[2:3], v[2:3], 0, s[14:15]
	v_or_b32_e32 v10, s45, v117
	v_lshl_add_u64 v[2:3], v[2:3], 0, v[100:101]
	v_mad_i64_i32 v[10:11], s[26:27], v10, s60, v[50:51]
	s_mul_i32 s4, s10, 0x110
	v_add_co_u32_e32 v6, vcc, s78, v2
	v_lshl_add_u64 v[10:11], v[10:11], 0, s[14:15]
	v_or_b32_e32 v18, s45, v118
	s_add_i32 s4, s4, s5
	v_addc_co_u32_e32 v7, vcc, 0, v3, vcc
	v_lshl_add_u64 v[10:11], v[10:11], 0, v[100:101]
	v_mad_i64_i32 v[18:19], s[26:27], v18, s60, v[50:51]
	s_add_i32 s4, s4, s11
	v_add_co_u32_e32 v14, vcc, s78, v10
	v_lshl_add_u64 v[18:19], v[18:19], 0, s[14:15]
	v_or_b32_e32 v26, s45, v119
	s_ashr_i32 s5, s4, 31
	v_addc_co_u32_e32 v15, vcc, 0, v11, vcc
	v_lshl_add_u64 v[18:19], v[18:19], 0, v[100:101]
	v_mad_i64_i32 v[26:27], s[26:27], v26, s60, v[50:51]
	s_lshl_b64 s[10:11], s[4:5], 13
	s_add_i32 s4, s4, 34
	v_add_co_u32_e32 v22, vcc, s78, v18
	v_lshl_add_u64 v[26:27], v[26:27], 0, s[14:15]
	s_ashr_i32 s5, s4, 31
	v_addc_co_u32_e32 v23, vcc, 0, v19, vcc
	v_lshl_add_u64 v[26:27], v[26:27], 0, v[100:101]
	s_lshl_b64 s[4:5], s[4:5], 13
	v_add_co_u32_e32 v30, vcc, s78, v26
	s_cmp_eq_u32 s33, 0
	s_nop 0
	v_addc_co_u32_e32 v31, vcc, 0, v27, vcc
	s_cselect_b64 vcc, -1, 0
	s_add_u32 s10, s66, s10
	s_addc_u32 s11, s67, s11
	s_add_u32 s4, s66, s4
	s_addc_u32 s5, s67, s5
	v_or_b32_e32 v104, s45, v109
	global_load_dwordx4 v[2:5], v[6:7], off offset:512
	s_nop 0
	global_load_dwordx4 v[6:9], v[6:7], off
	s_nop 0
	global_load_dwordx4 v[10:13], v[14:15], off offset:512
	s_nop 0
	global_load_dwordx4 v[14:17], v[14:15], off
	s_nop 0
	global_load_dwordx4 v[18:21], v[22:23], off offset:512
	s_nop 0
	global_load_dwordx4 v[22:25], v[22:23], off
	s_nop 0
	global_load_dwordx4 v[26:29], v[30:31], off offset:512
	s_nop 0
	global_load_dwordx4 v[30:33], v[30:31], off
	s_nop 0
	global_load_dwordx4 v[34:37], v125, s[10:11]
	global_load_dwordx4 v[38:41], v125, s[4:5]
	global_load_dwordx4 v[42:45], v126, s[10:11]
	global_load_dwordx4 v[46:49], v126, s[4:5]
	v_mad_i64_i32 v[106:107], s[4:5], v104, s60, v[50:51]
	v_lshl_add_u64 v[50:51], v[106:107], 0, s[14:15]
	v_mov_b32_e32 v103, v0
	v_lshl_add_u64 v[50:51], v[50:51], 0, v[102:103]
	global_load_dwordx4 v[78:81], v[50:51], off offset:3584
	global_load_dwordx4 v[74:77], v[50:51], off offset:3616
	global_load_dwordx4 v[70:73], v[50:51], off offset:3648
	global_load_dwordx4 v[66:69], v[50:51], off offset:3680
	v_cndmask_b32_e32 v50, v142, v1, vcc
	s_mov_b32 s10, 0
	v_mul_f32_e32 v101, 0xbfb8aa3b, v50
	v_ashrrev_i32_e32 v105, 31, v104
	s_mov_b64 s[4:5], -1
	s_waitcnt vmcnt(15)
	ds_write_b128 v127, v[2:5]
	s_waitcnt vmcnt(14)
	ds_write_b128 v128, v[6:9] offset:16384
	s_waitcnt vmcnt(13)
	ds_write_b128 v129, v[10:13]
	s_waitcnt vmcnt(12)
	ds_write_b128 v130, v[14:17] offset:16384
	s_waitcnt vmcnt(11)
	ds_write_b128 v127, v[18:21] offset:8192
	s_waitcnt vmcnt(10)
	ds_write_b128 v131, v[22:25] offset:16384
	s_waitcnt vmcnt(9)
	ds_write_b128 v132, v[26:29] offset:8192
	s_waitcnt vmcnt(8)
	ds_write_b128 v133, v[30:33] offset:16384
	s_waitcnt vmcnt(7)
	ds_write_b128 v128, v[34:37] offset:32768
	s_waitcnt vmcnt(6)
	ds_write_b128 v128, v[38:41] offset:40960
	s_waitcnt vmcnt(5)
	ds_write_b128 v130, v[42:45] offset:32768
	s_waitcnt vmcnt(4)
	ds_write_b128 v130, v[46:49] offset:40960
	v_cndmask_b32_e32 v2, v143, v141, vcc
	v_mov_b32_e32 v18, 0
	v_mul_f32_e32 v103, 0xbfb8aa3b, v2
	v_mul_f32_e32 v167, 0xbf800000, v101
	v_mul_f32_e32 v168, 0xc0000000, v101
	v_mul_f32_e32 v169, 0xc0400000, v101
	v_mul_f32_e32 v170, 0xc1000000, v101
	v_mul_f32_e32 v171, 0x3f800000, v103
	v_mul_f32_e32 v172, 0x40000000, v103
	v_mul_f32_e32 v173, 0x40400000, v103
	v_mul_f32_e32 v174, 0x41000000, v103
	v_exp_f32_e32 v167, v167
	v_exp_f32_e32 v168, v168
	v_exp_f32_e32 v169, v169
	v_exp_f32_e32 v170, v170
	v_exp_f32_e32 v171, v171
	v_exp_f32_e32 v172, v172
	v_exp_f32_e32 v173, v173
	v_exp_f32_e32 v174, v174
	v_mov_b32_e32 v19, v18
	v_mov_b32_e32 v20, v18
	v_mov_b32_e32 v21, v18
	v_mov_b32_e32 v22, v18
	v_mov_b32_e32 v23, v18
	v_mov_b32_e32 v24, v18
	v_mov_b32_e32 v25, v18
	v_mov_b32_e32 v26, v18
	v_mov_b32_e32 v27, v18
	v_mov_b32_e32 v28, v18
	v_mov_b32_e32 v29, v18
	v_mov_b32_e32 v30, v18
	v_mov_b32_e32 v31, v18
	v_mov_b32_e32 v32, v18
	v_mov_b32_e32 v33, v18
	v_mov_b32_e32 v2, v18
	v_mov_b32_e32 v3, v18
	v_mov_b32_e32 v4, v18
	v_mov_b32_e32 v5, v18
	v_mov_b32_e32 v6, v18
	v_mov_b32_e32 v7, v18
	v_mov_b32_e32 v8, v18
	v_mov_b32_e32 v9, v18
	v_mov_b32_e32 v10, v18
	v_mov_b32_e32 v11, v18
	v_mov_b32_e32 v12, v18
	v_mov_b32_e32 v13, v18
	v_mov_b32_e32 v14, v18
	v_mov_b32_e32 v15, v18
	v_mov_b32_e32 v16, v18
	v_mov_b32_e32 v17, v18
	s_waitcnt lgkmcnt(0)
	s_barrier
.LBB0_556:
	v_cndmask_b32_e64 v34, 0, 1, s[4:5]
	s_lshl_b32 s4, s10, 6
	v_cmp_ne_u32_e32 vcc, 1, v34
	v_or_b32_e32 v34, s4, v108
	v_lshl_add_u32 v152, v34, 7, s58
	v_add_u32_e32 v38, v152, v120
	ds_read_b128 v[34:37], v38 offset:16384
	ds_read_b128 v[50:53], v38 offset:20480
	v_add_u32_e32 v148, v152, v121
	s_waitcnt vmcnt(3) lgkmcnt(1)
	v_mfma_f32_32x32x16_bf16 v[34:49], v[34:37], v[78:81], 0
	ds_read_b128 v[144:147], v148 offset:16384
	ds_read_b128 v[148:151], v148 offset:20480
	s_waitcnt lgkmcnt(2)
	v_mfma_f32_32x32x16_bf16 v[50:65], v[50:53], v[78:81], 0
	s_waitcnt vmcnt(2) lgkmcnt(1)
	v_mfma_f32_32x32x16_bf16 v[34:49], v[144:147], v[74:77], v[34:49]
	s_waitcnt lgkmcnt(0)
	v_mfma_f32_32x32x16_bf16 v[50:65], v[148:151], v[74:77], v[50:65]
	v_add_u32_e32 v148, v152, v122
	ds_read_b128 v[144:147], v148 offset:16384
	ds_read_b128 v[148:151], v148 offset:20480
	s_waitcnt vmcnt(1) lgkmcnt(1)
	v_mfma_f32_32x32x16_bf16 v[34:49], v[144:147], v[70:73], v[34:49]
	s_waitcnt lgkmcnt(0)
	v_mfma_f32_32x32x16_bf16 v[50:65], v[148:151], v[70:73], v[50:65]
	v_add_u32_e32 v148, v152, v123
	ds_read_b128 v[144:147], v148 offset:16384
	ds_read_b128 v[148:151], v148 offset:20480
	s_waitcnt vmcnt(0) lgkmcnt(1)
	v_mfma_f32_32x32x16_bf16 v[34:49], v[144:147], v[66:69], v[34:49]
	v_or_b32_e32 v145, s4, v82
	s_waitcnt lgkmcnt(0)
	v_mfma_f32_32x32x16_bf16 v[50:65], v[148:151], v[66:69], v[50:65]
	v_sub_u32_e32 v166, v109, v145
	v_cvt_f32_i32_e32 v166, v166
	v_mul_f32_e32 v175, v101, v166
	v_mul_f32_e64 v183, -v103, v166
	v_exp_f32_e32 v175, v175
	v_exp_f32_e32 v183, v183
	s_nop 0
	v_mul_f32_e32 v176, v175, v170
	v_mul_f32_e32 v184, v183, v174
	v_mul_f32_e32 v177, v176, v170
	v_mul_f32_e32 v185, v184, v174
	v_mul_f32_e32 v178, v177, v170
	v_mul_f32_e32 v186, v185, v174
	v_mul_f32_e32 v179, v178, v170
	v_mul_f32_e32 v187, v186, v174
	v_mul_f32_e32 v180, v179, v170
	v_mul_f32_e32 v188, v187, v174
	v_mul_f32_e32 v181, v180, v170
	v_mul_f32_e32 v189, v188, v174
	v_mul_f32_e32 v182, v181, v170
	v_mul_f32_e32 v190, v189, v174
	v_min_f32_e32 v160, v175, v183
	v_mul_f32_e32 v144, v34, v160
	v_min_f32_e32 v162, v179, v187
	v_mul_f32_e32 v34, v50, v162
	v_mul_f32_e32 v164, v175, v167
	v_mul_f32_e32 v165, v183, v171
	v_min_f32_e32 v164, v164, v165
	v_mul_f32_e32 v50, v35, v164
	v_mul_f32_e32 v160, v179, v167
	v_mul_f32_e32 v161, v187, v171
	v_min_f32_e32 v160, v160, v161
	v_mul_f32_e32 v35, v51, v160
	v_mul_f32_e32 v162, v175, v168
	v_mul_f32_e32 v163, v183, v172
	v_min_f32_e32 v162, v162, v163
	v_mul_f32_e32 v51, v36, v162
	v_mul_f32_e32 v164, v179, v168
	v_mul_f32_e32 v165, v187, v172
	v_min_f32_e32 v164, v164, v165
	v_mul_f32_e32 v36, v52, v164
	v_mul_f32_e32 v160, v175, v169
	v_mul_f32_e32 v161, v183, v173
	v_min_f32_e32 v160, v160, v161
	v_mul_f32_e32 v52, v37, v160
	v_mul_f32_e32 v162, v179, v169
	v_mul_f32_e32 v163, v187, v173
	v_min_f32_e32 v162, v162, v163
	v_mul_f32_e32 v37, v53, v162
	v_min_f32_e32 v164, v176, v184
	v_mul_f32_e32 v53, v38, v164
	v_min_f32_e32 v160, v180, v188
	v_mul_f32_e32 v38, v54, v160
	v_mul_f32_e32 v162, v176, v167
	v_mul_f32_e32 v163, v184, v171
	v_min_f32_e32 v162, v162, v163
	v_mul_f32_e32 v54, v39, v162
	v_mul_f32_e32 v164, v180, v167
	v_mul_f32_e32 v165, v188, v171
	v_min_f32_e32 v164, v164, v165
	v_mul_f32_e32 v39, v55, v164
	v_mul_f32_e32 v160, v176, v168
	v_mul_f32_e32 v161, v184, v172
	v_min_f32_e32 v160, v160, v161
	v_mul_f32_e32 v55, v40, v160
	v_mul_f32_e32 v162, v180, v168
	v_mul_f32_e32 v163, v188, v172
	v_min_f32_e32 v162, v162, v163
	v_mul_f32_e32 v40, v56, v162
	v_mul_f32_e32 v164, v176, v169
	v_mul_f32_e32 v165, v184, v173
	v_min_f32_e32 v164, v164, v165
	v_mul_f32_e32 v56, v41, v164
	v_mul_f32_e32 v160, v180, v169
	v_mul_f32_e32 v161, v188, v173
	v_min_f32_e32 v160, v160, v161
	v_mul_f32_e32 v41, v57, v160
	v_min_f32_e32 v162, v177, v185
	v_mul_f32_e32 v57, v42, v162
	v_min_f32_e32 v164, v181, v189
	v_mul_f32_e32 v42, v58, v164
	v_mul_f32_e32 v160, v177, v167
	v_mul_f32_e32 v161, v185, v171
	v_min_f32_e32 v160, v160, v161
	v_mul_f32_e32 v43, v43, v160
	v_mul_f32_e32 v162, v181, v167
	v_mul_f32_e32 v163, v189, v171
	v_min_f32_e32 v162, v162, v163
	v_mul_f32_e32 v58, v59, v162
	v_mul_f32_e32 v164, v177, v168
	v_mul_f32_e32 v165, v185, v172
	v_min_f32_e32 v164, v164, v165
	v_mul_f32_e32 v59, v44, v164
	v_mul_f32_e32 v160, v181, v168
	v_mul_f32_e32 v161, v189, v172
	v_min_f32_e32 v160, v160, v161
	v_mul_f32_e32 v60, v60, v160
	v_mul_f32_e32 v162, v177, v169
	v_mul_f32_e32 v163, v185, v173
	v_min_f32_e32 v162, v162, v163
	v_mul_f32_e32 v147, v45, v162
	v_mul_f32_e32 v164, v181, v169
	v_mul_f32_e32 v165, v189, v173
	v_min_f32_e32 v164, v164, v165
	v_mul_f32_e32 v61, v61, v164
	v_min_f32_e32 v160, v178, v186
	v_mul_f32_e32 v146, v46, v160
	v_min_f32_e32 v162, v182, v190
	v_mul_f32_e32 v62, v62, v162
	v_mul_f32_e32 v164, v178, v167
	v_mul_f32_e32 v165, v186, v171
	v_min_f32_e32 v164, v164, v165
	v_mul_f32_e32 v148, v47, v164
	v_mul_f32_e32 v160, v182, v167
	v_mul_f32_e32 v161, v190, v171
	v_min_f32_e32 v160, v160, v161
	v_mul_f32_e32 v63, v63, v160
	v_mul_f32_e32 v162, v178, v168
	v_mul_f32_e32 v163, v186, v172
	v_min_f32_e32 v162, v162, v163
	v_mul_f32_e32 v149, v48, v162
	v_mul_f32_e32 v164, v182, v168
	v_mul_f32_e32 v165, v190, v172
	v_min_f32_e32 v164, v164, v165
	v_mul_f32_e32 v64, v64, v164
	v_mul_f32_e32 v160, v178, v169
	v_mul_f32_e32 v161, v186, v173
	v_min_f32_e32 v160, v160, v161
	v_mul_f32_e32 v145, v49, v160
	v_mul_f32_e32 v162, v182, v169
	v_mul_f32_e32 v163, v190, v173
	v_min_f32_e32 v162, v162, v163
	v_mul_f32_e32 v65, v65, v162
	v_cvt_pk_bf16_f32 v44, v144, v50
	v_cvt_pk_bf16_f32 v45, v51, v52
	v_cvt_pk_bf16_f32 v46, v53, v54
	v_cvt_pk_bf16_f32 v47, v55, v56
	v_cvt_pk_bf16_f32 v48, v57, v43
	v_cvt_pk_bf16_f32 v49, v59, v147
	v_cvt_pk_bf16_f32 v50, v146, v148
	v_cvt_pk_bf16_f32 v51, v149, v145
	v_cvt_pk_bf16_f32 v34, v34, v35
	v_cvt_pk_bf16_f32 v35, v36, v37
	v_cvt_pk_bf16_f32 v36, v38, v39
	v_cvt_pk_bf16_f32 v37, v40, v41
	v_cvt_pk_bf16_f32 v38, v42, v58
	v_cvt_pk_bf16_f32 v39, v60, v61
	v_cvt_pk_bf16_f32 v40, v62, v63
	v_cvt_pk_bf16_f32 v41, v64, v65
	v_lshl_add_u32 v42, s10, 13, v110
	ds_read_b64_tr_b16 v[52:53], v42 offset:0
	ds_read_b64_tr_b16 v[54:55], v42 offset:0x400
	ds_read_b64_tr_b16 v[56:57], v42 offset:0x800
	ds_read_b64_tr_b16 v[58:59], v42 offset:0xc00
	ds_read_b64_tr_b16 v[60:61], v42 offset:0x1000
	ds_read_b64_tr_b16 v[62:63], v42 offset:0x1400
	ds_read_b64_tr_b16 v[144:145], v42 offset:0x1800
	ds_read_b64_tr_b16 v[146:147], v42 offset:0x1c00
	s_waitcnt lgkmcnt(0)
	v_permlane32_swap_b32_e32 v44, v46
	v_permlane32_swap_b32_e32 v45, v47
	v_permlane32_swap_b32_e32 v48, v50
	v_permlane32_swap_b32_e32 v49, v51
	v_permlane32_swap_b32_e32 v34, v36
	v_permlane32_swap_b32_e32 v35, v37
	v_permlane32_swap_b32_e32 v38, v40
	v_permlane32_swap_b32_e32 v39, v41
	v_mfma_f32_32x32x16_bf16 v[18:33], v[52:55], v[44:47], v[18:33]
	ds_read_b64_tr_b16 v[52:53], v42 offset:0x200
	ds_read_b64_tr_b16 v[54:55], v42 offset:0x600
	v_mfma_f32_32x32x16_bf16 v[18:33], v[56:59], v[48:51], v[18:33]
	ds_read_b64_tr_b16 v[56:57], v42 offset:0xa00
	ds_read_b64_tr_b16 v[58:59], v42 offset:0xe00
	v_mfma_f32_32x32x16_bf16 v[18:33], v[60:63], v[34:37], v[18:33]
	ds_read_b64_tr_b16 v[60:61], v42 offset:0x1200
	ds_read_b64_tr_b16 v[62:63], v42 offset:0x1600
	v_mfma_f32_32x32x16_bf16 v[18:33], v[144:147], v[38:41], v[18:33]
	ds_read_b64_tr_b16 v[144:145], v42 offset:0x1a00
	ds_read_b64_tr_b16 v[146:147], v42 offset:0x1e00
	s_waitcnt lgkmcnt(0)
	v_mfma_f32_32x32x16_bf16 v[2:17], v[52:55], v[44:47], v[2:17]
	s_mov_b64 s[4:5], 0
	s_and_b64 vcc, exec, vcc
	s_mov_b32 s10, 1
	v_mfma_f32_32x32x16_bf16 v[2:17], v[56:59], v[48:51], v[2:17]
	v_mfma_f32_32x32x16_bf16 v[2:17], v[60:63], v[34:37], v[2:17]
	v_mfma_f32_32x32x16_bf16 v[2:17], v[144:147], v[38:41], v[2:17]
	s_cbranch_vccz .LBB0_556
	v_mul_f32_e32 v34, v101, v111
	v_exp_f32_e32 v50, v34
	v_mul_f32_e32 v34, v103, v112
	v_exp_f32_e32 v51, v34
	v_lshlrev_b32_e32 v35, 16, v78
	v_and_b32_e32 v36, 0xffff0000, v78
	v_mul_f32_e32 v34, v50, v35
	v_mul_f32_e32 v37, v50, v36
	v_mul_f32_e32 v36, v51, v36
	v_cvt_pk_bf16_f32 v34, v34, v37
	v_mul_f32_e32 v35, v51, v35
	v_cvt_pk_bf16_f32 v38, v35, v36
	v_lshlrev_b32_e32 v36, 16, v79
	v_and_b32_e32 v37, 0xffff0000, v79
	v_mul_f32_e32 v35, v50, v36
	v_mul_f32_e32 v39, v50, v37
	v_mul_f32_e32 v37, v51, v37
	v_cvt_pk_bf16_f32 v35, v35, v39
	v_mul_f32_e32 v36, v51, v36
	v_cvt_pk_bf16_f32 v39, v36, v37
	v_lshlrev_b32_e32 v37, 16, v80
	v_and_b32_e32 v40, 0xffff0000, v80
	v_mul_f32_e32 v36, v50, v37
	v_mul_f32_e32 v41, v50, v40
	v_cvt_pk_bf16_f32 v36, v36, v41
	v_mul_f32_e32 v37, v51, v37
	v_mul_f32_e32 v40, v51, v40
	v_lshlrev_b32_e32 v41, 16, v81
	v_and_b32_e32 v42, 0xffff0000, v81
	v_cvt_pk_bf16_f32 v40, v37, v40
	v_mul_f32_e32 v37, v50, v41
	v_mul_f32_e32 v43, v50, v42
	v_mul_f32_e32 v41, v51, v41
	v_mul_f32_e32 v42, v51, v42
	v_cvt_pk_bf16_f32 v37, v37, v43
	v_cvt_pk_bf16_f32 v41, v41, v42
	ds_read_b128 v[42:45], v134 offset:32768
	ds_read_b128 v[46:49], v134 offset:40960
	s_waitcnt lgkmcnt(1)
	v_mfma_f32_32x32x16_bf16 v[18:33], v[42:45], v[34:37], v[18:33]
	s_mov_b64 s[4:5], 0x1400
	s_waitcnt lgkmcnt(0)
	v_mfma_f32_32x32x16_bf16 v[18:33], v[46:49], v[38:41], v[18:33]
	ds_read_b128 v[42:45], v134 offset:36864
	ds_read_b128 v[46:49], v134 offset:45056
	s_waitcnt lgkmcnt(1)
	v_mfma_f32_32x32x16_bf16 v[2:17], v[42:45], v[34:37], v[2:17]
	v_lshlrev_b32_e32 v35, 16, v74
	v_and_b32_e32 v36, 0xffff0000, v74
	v_mul_f32_e32 v34, v50, v35
	v_mul_f32_e32 v37, v50, v36
	v_mul_f32_e32 v36, v51, v36
	v_cvt_pk_bf16_f32 v34, v34, v37
	v_mul_f32_e32 v35, v51, v35
	s_waitcnt lgkmcnt(0)
	v_mfma_f32_32x32x16_bf16 v[2:17], v[46:49], v[38:41], v[2:17]
	v_cvt_pk_bf16_f32 v38, v35, v36
	v_lshlrev_b32_e32 v36, 16, v75
	v_and_b32_e32 v37, 0xffff0000, v75
	v_mul_f32_e32 v35, v50, v36
	v_mul_f32_e32 v39, v50, v37
	v_mul_f32_e32 v37, v51, v37
	v_cvt_pk_bf16_f32 v35, v35, v39
	v_mul_f32_e32 v36, v51, v36
	v_cvt_pk_bf16_f32 v39, v36, v37
	v_lshlrev_b32_e32 v37, 16, v76
	v_and_b32_e32 v40, 0xffff0000, v76
	v_mul_f32_e32 v36, v50, v37
	v_mul_f32_e32 v41, v50, v40
	v_cvt_pk_bf16_f32 v36, v36, v41
	v_mul_f32_e32 v37, v51, v37
	v_mul_f32_e32 v40, v51, v40
	v_lshlrev_b32_e32 v41, 16, v77
	v_and_b32_e32 v42, 0xffff0000, v77
	v_cvt_pk_bf16_f32 v40, v37, v40
	v_mul_f32_e32 v37, v50, v41
	v_mul_f32_e32 v43, v50, v42
	v_mul_f32_e32 v41, v51, v41
	v_mul_f32_e32 v42, v51, v42
	v_cvt_pk_bf16_f32 v37, v37, v43
	v_cvt_pk_bf16_f32 v41, v41, v42
	ds_read_b128 v[42:45], v135 offset:32768
	ds_read_b128 v[46:49], v135 offset:40960
	s_waitcnt lgkmcnt(1)
	v_mfma_f32_32x32x16_bf16 v[18:33], v[42:45], v[34:37], v[18:33]
	s_waitcnt lgkmcnt(0)
	v_mfma_f32_32x32x16_bf16 v[18:33], v[46:49], v[38:41], v[18:33]
	ds_read_b128 v[42:45], v135 offset:36864
	ds_read_b128 v[46:49], v135 offset:45056
	s_waitcnt lgkmcnt(1)
	v_mfma_f32_32x32x16_bf16 v[2:17], v[42:45], v[34:37], v[2:17]
	v_lshlrev_b32_e32 v35, 16, v70
	v_and_b32_e32 v36, 0xffff0000, v70
	v_mul_f32_e32 v34, v50, v35
	v_mul_f32_e32 v37, v50, v36
	v_mul_f32_e32 v36, v51, v36
	v_cvt_pk_bf16_f32 v34, v34, v37
	v_mul_f32_e32 v35, v51, v35
	s_waitcnt lgkmcnt(0)
	v_mfma_f32_32x32x16_bf16 v[2:17], v[46:49], v[38:41], v[2:17]
	v_cvt_pk_bf16_f32 v38, v35, v36
	v_lshlrev_b32_e32 v36, 16, v71
	v_and_b32_e32 v37, 0xffff0000, v71
	v_mul_f32_e32 v35, v50, v36
	v_mul_f32_e32 v39, v50, v37
	v_mul_f32_e32 v37, v51, v37
	v_cvt_pk_bf16_f32 v35, v35, v39
	v_mul_f32_e32 v36, v51, v36
	v_cvt_pk_bf16_f32 v39, v36, v37
	v_lshlrev_b32_e32 v37, 16, v72
	v_and_b32_e32 v40, 0xffff0000, v72
	v_mul_f32_e32 v36, v50, v37
	v_mul_f32_e32 v41, v50, v40
	v_cvt_pk_bf16_f32 v36, v36, v41
	v_mul_f32_e32 v37, v51, v37
	v_mul_f32_e32 v40, v51, v40
	v_lshlrev_b32_e32 v41, 16, v73
	v_and_b32_e32 v42, 0xffff0000, v73
	v_cvt_pk_bf16_f32 v40, v37, v40
	v_mul_f32_e32 v37, v50, v41
	v_mul_f32_e32 v43, v50, v42
	v_mul_f32_e32 v41, v51, v41
	v_mul_f32_e32 v42, v51, v42
	v_cvt_pk_bf16_f32 v37, v37, v43
	v_cvt_pk_bf16_f32 v41, v41, v42
	ds_read_b128 v[42:45], v136 offset:32768
	ds_read_b128 v[46:49], v136 offset:40960
	s_waitcnt lgkmcnt(1)
	v_mfma_f32_32x32x16_bf16 v[18:33], v[42:45], v[34:37], v[18:33]
	s_waitcnt lgkmcnt(0)
	v_mfma_f32_32x32x16_bf16 v[18:33], v[46:49], v[38:41], v[18:33]
	ds_read_b128 v[42:45], v136 offset:36864
	ds_read_b128 v[46:49], v136 offset:45056
	s_waitcnt lgkmcnt(1)
	v_mfma_f32_32x32x16_bf16 v[2:17], v[42:45], v[34:37], v[2:17]
	v_lshlrev_b32_e32 v35, 16, v66
	v_and_b32_e32 v36, 0xffff0000, v66
	v_mul_f32_e32 v34, v50, v35
	v_mul_f32_e32 v37, v50, v36
	v_mul_f32_e32 v36, v51, v36
	v_cvt_pk_bf16_f32 v34, v34, v37
	v_mul_f32_e32 v35, v51, v35
	s_waitcnt lgkmcnt(0)
	v_mfma_f32_32x32x16_bf16 v[2:17], v[46:49], v[38:41], v[2:17]
	v_cvt_pk_bf16_f32 v38, v35, v36
	v_lshlrev_b32_e32 v36, 16, v67
	v_and_b32_e32 v37, 0xffff0000, v67
	v_mul_f32_e32 v35, v50, v36
	v_mul_f32_e32 v39, v50, v37
	v_mul_f32_e32 v37, v51, v37
	v_cvt_pk_bf16_f32 v35, v35, v39
	v_mul_f32_e32 v36, v51, v36
	v_cvt_pk_bf16_f32 v39, v36, v37
	v_lshlrev_b32_e32 v37, 16, v68
	v_and_b32_e32 v40, 0xffff0000, v68
	v_mul_f32_e32 v36, v50, v37
	v_mul_f32_e32 v41, v50, v40
	v_cvt_pk_bf16_f32 v36, v36, v41
	v_mul_f32_e32 v37, v51, v37
	v_mul_f32_e32 v40, v51, v40
	v_lshlrev_b32_e32 v41, 16, v69
	v_and_b32_e32 v42, 0xffff0000, v69
	v_cvt_pk_bf16_f32 v40, v37, v40
	v_mul_f32_e32 v37, v50, v41
	v_mul_f32_e32 v43, v50, v42
	v_mul_f32_e32 v41, v51, v41
	v_mul_f32_e32 v42, v51, v42
	v_cvt_pk_bf16_f32 v37, v37, v43
	v_cvt_pk_bf16_f32 v41, v41, v42
	ds_read_b128 v[42:45], v137 offset:32768
	ds_read_b128 v[46:49], v137 offset:40960
	s_waitcnt lgkmcnt(1)
	v_mfma_f32_32x32x16_bf16 v[18:33], v[42:45], v[34:37], v[18:33]
	s_waitcnt lgkmcnt(0)
	v_mfma_f32_32x32x16_bf16 v[18:33], v[46:49], v[38:41], v[18:33]
	ds_read_b128 v[42:45], v137 offset:36864
	ds_read_b128 v[46:49], v137 offset:45056
	s_waitcnt lgkmcnt(1)
	v_mfma_f32_32x32x16_bf16 v[2:17], v[42:45], v[34:37], v[2:17]
	v_lshl_add_u64 v[34:35], s[22:23], 1, v[106:107]
	v_lshlrev_b32_e32 v36, 1, v82
	v_mov_b32_e32 v37, v0
	v_lshl_add_u64 v[34:35], v[34:35], 0, v[36:37]
	v_lshl_add_u64 v[36:37], v[34:35], 0, s[4:5]
	v_add_co_u32_e32 v34, vcc, s78, v34
	s_lshl_b64 s[4:5], s[24:25], 2
	s_nop 0
	v_addc_co_u32_e32 v35, vcc, 0, v35, vcc
	global_load_dwordx2 v[80:81], v[34:35], off offset:1024
	global_load_dwordx2 v[76:77], v[36:37], off offset:16
	global_load_dwordx2 v[74:75], v[36:37], off offset:32
	global_load_dwordx2 v[72:73], v[36:37], off offset:48
	global_load_dwordx2 v[70:71], v[36:37], off offset:64
	global_load_dwordx2 v[68:69], v[36:37], off offset:80
	global_load_dwordx2 v[66:67], v[36:37], off offset:96
	global_load_dwordx2 v[64:65], v[36:37], off offset:112
	ds_read_b32 v34, v0 offset:640
	ds_read_b32 v35, v0 offset:644
	s_waitcnt lgkmcnt(2)
	v_mfma_f32_32x32x16_bf16 v[2:17], v[46:49], v[38:41], v[2:17]
	v_mul_f32_e32 v78, v19, v19
	v_fmac_f32_e32 v78, v18, v18
	s_waitcnt lgkmcnt(1)
	v_readfirstlane_b32 s11, v34
	s_waitcnt lgkmcnt(0)
	v_readfirstlane_b32 s10, v35
	s_add_u32 s11, s11, s4
	s_addc_u32 s10, s10, s5
	s_lshl_b64 s[4:5], s[22:23], 2
	s_add_u32 s4, s11, s4
	s_addc_u32 s5, s10, s5
	v_lshlrev_b32_e32 v34, 2, v82
	global_load_dwordx4 v[144:147], v34, s[4:5]
	global_load_dwordx4 v[58:61], v34, s[4:5] offset:32
	global_load_dwordx4 v[54:57], v34, s[4:5] offset:64
	global_load_dwordx4 v[50:53], v34, s[4:5] offset:96
	global_load_dwordx4 v[46:49], v34, s[4:5] offset:128
	global_load_dwordx4 v[42:45], v34, s[4:5] offset:160
	global_load_dwordx4 v[38:41], v34, s[4:5] offset:192
	s_nop 0
	global_load_dwordx4 v[34:37], v34, s[4:5] offset:224
	v_fmac_f32_e32 v78, v20, v20
	v_fmac_f32_e32 v78, v21, v21
	v_fmac_f32_e32 v78, v22, v22
	v_fmac_f32_e32 v78, v23, v23
	v_fmac_f32_e32 v78, v24, v24
	v_fmac_f32_e32 v78, v25, v25
	v_fmac_f32_e32 v78, v26, v26
	v_fmac_f32_e32 v78, v27, v27
	v_fmac_f32_e32 v78, v28, v28
	v_fmac_f32_e32 v78, v29, v29
	v_fmac_f32_e32 v78, v30, v30
	v_fmac_f32_e32 v78, v31, v31
	v_fmac_f32_e32 v78, v32, v32
	v_fmac_f32_e32 v78, v33, v33
	v_fmac_f32_e32 v78, v2, v2
	v_fmac_f32_e32 v78, v3, v3
	v_fmac_f32_e32 v78, v4, v4
	v_fmac_f32_e32 v78, v5, v5
	v_fmac_f32_e32 v78, v6, v6
	v_fmac_f32_e32 v78, v7, v7
	v_fmac_f32_e32 v78, v8, v8
	v_fmac_f32_e32 v78, v9, v9
	v_fmac_f32_e32 v78, v10, v10
	v_fmac_f32_e32 v78, v11, v11
	v_fmac_f32_e32 v78, v12, v12
	v_fmac_f32_e32 v78, v13, v13
	v_fmac_f32_e32 v78, v14, v14
	v_fmac_f32_e32 v78, v15, v15
	v_pk_mul_f32 v[62:63], v[16:17], v[16:17]
	s_and_b64 vcc, exec, s[20:21]
	v_add_f32_e32 v62, v78, v62
	v_add_f32_e32 v62, v62, v63
	v_mov_b32_e32 v63, v62
	s_nop 1
	v_permlane32_swap_b32_e32 v62, v63
	v_add_f32_e32 v62, v62, v63
	v_fmamk_f32 v62, v62, 0x3c800000, v210
	v_rsq_f32_e32 v78, v62
	v_lshlrev_b64 v[62:63], 10, v[104:105]
	v_lshl_add_u64 v[62:63], s[82:83], 0, v[62:63]
	v_lshl_add_u64 v[62:63], v[62:63], 0, s[22:23]
	v_mul_f32_e32 v78, 0x41800000, v78
	v_mul_f32_e32 v150, v78, v18
	v_lshl_add_u64 v[62:63], v[62:63], 0, v[84:85]
	s_waitcnt vmcnt(15)
	v_lshlrev_b32_e32 v105, 16, v80
	v_mul_f32_e32 v79, 0xbfb8aa3b, v105
	v_exp_f32_e32 v79, v79
	v_and_b32_e32 v107, 0xffff0000, v80
	v_mul_f32_e32 v18, 0xbfb8aa3b, v107
	v_exp_f32_e32 v18, v18
	v_add_f32_e32 v79, 1.0, v79
	v_rcp_f32_e32 v151, v79
	v_lshlrev_b32_e32 v149, 16, v81
	v_add_f32_e32 v18, 1.0, v18
	v_and_b32_e32 v81, 0xffff0000, v81
	s_waitcnt vmcnt(7)
	v_mov_b32_e32 v104, v144
	v_pk_mul_f32 v[104:105], v[150:151], v[104:105]
	v_mov_b32_e32 v106, v145
	v_mul_f32_e32 v79, v104, v105
	v_rcp_f32_e32 v105, v18
	v_mul_f32_e32 v104, v78, v19
	v_mov_b32_e32 v148, v146
	v_mov_b32_e32 v80, v147
	v_pk_mul_f32 v[18:19], v[104:105], v[106:107]
	v_mul_f32_e32 v106, v78, v22
	v_mul_f32_e32 v101, v18, v19
	v_mul_f32_e32 v18, 0xbfb8aa3b, v149
	v_exp_f32_e32 v18, v18
	v_lshlrev_b32_e32 v105, 16, v77
	s_waitcnt vmcnt(6)
	v_mov_b32_e32 v104, v60
	v_and_b32_e32 v77, 0xffff0000, v77
	v_add_f32_e32 v18, 1.0, v18
	v_rcp_f32_e32 v19, v18
	v_mul_f32_e32 v18, v78, v20
	s_waitcnt vmcnt(5)
	v_mov_b32_e32 v60, v57
	v_pk_mul_f32 v[18:19], v[18:19], v[148:149]
	s_nop 0
	v_mul_f32_e32 v20, v18, v19
	v_mul_f32_e32 v18, 0xbfb8aa3b, v81
	v_exp_f32_e32 v18, v18
	s_nop 0
	v_add_f32_e32 v18, 1.0, v18
	v_rcp_f32_e32 v19, v18
	v_mul_f32_e32 v18, v78, v21
	v_lshlrev_b32_e32 v21, 16, v76
	v_pk_mul_f32 v[18:19], v[18:19], v[80:81]
	s_nop 0
	v_mul_f32_e32 v19, v18, v19
	v_cvt_pk_fp8_f32 v18, v79, v101
	v_and_b32_e32 v81, 0xffff0000, v76
	v_mov_b32_e32 v80, v59
	v_mov_b32_e32 v76, v61
	v_cvt_pk_fp8_f32 v18, v20, v19 op_sel:[0,0,1]
	v_mul_f32_e32 v19, 0xbfb8aa3b, v21
	v_exp_f32_e32 v19, v19
	v_mov_b32_e32 v20, v58
	v_lshlrev_b32_e32 v59, 16, v75
	v_and_b32_e32 v61, 0xffff0000, v75
	v_add_f32_e32 v19, 1.0, v19
	v_rcp_f32_e32 v107, v19
	v_mov_b32_e32 v58, v56
	v_pk_mul_f32 v[20:21], v[106:107], v[20:21]
	s_nop 0
	v_mul_f32_e32 v19, v20, v21
	v_mul_f32_e32 v20, 0xbfb8aa3b, v81
	v_exp_f32_e32 v20, v20
	s_nop 0
	v_add_f32_e32 v20, 1.0, v20
	v_rcp_f32_e32 v21, v20
	v_mul_f32_e32 v20, v78, v23
	v_pk_mul_f32 v[20:21], v[20:21], v[80:81]
	s_nop 0
	v_mul_f32_e32 v22, v20, v21
	v_mul_f32_e32 v20, 0xbfb8aa3b, v105
	v_exp_f32_e32 v20, v20
	s_nop 0
	v_add_f32_e32 v20, 1.0, v20
	v_rcp_f32_e32 v21, v20
	v_mul_f32_e32 v20, v78, v24
	v_mov_b32_e32 v24, v55
	v_pk_mul_f32 v[20:21], v[20:21], v[104:105]
	s_nop 0
	v_mul_f32_e32 v23, v20, v21
	v_mul_f32_e32 v20, 0xbfb8aa3b, v77
	v_exp_f32_e32 v20, v20
	s_nop 0
	v_add_f32_e32 v20, 1.0, v20
	v_rcp_f32_e32 v21, v20
	v_mul_f32_e32 v20, v78, v25
	v_and_b32_e32 v25, 0xffff0000, v74
	v_pk_mul_f32 v[20:21], v[20:21], v[76:77]
	s_nop 0
	v_mul_f32_e32 v21, v20, v21
	v_cvt_pk_fp8_f32 v20, v19, v22
	v_mov_b32_e32 v22, v54
	v_mul_f32_e32 v54, v78, v30
	v_cvt_pk_fp8_f32 v20, v23, v21 op_sel:[0,0,1]
	v_lshlrev_b32_e32 v23, 16, v74
	v_mul_f32_e32 v19, 0xbfb8aa3b, v23
	v_exp_f32_e32 v19, v19
	v_mul_f32_e32 v74, v78, v26
	s_waitcnt vmcnt(4)
	v_mov_b32_e32 v26, v52
	v_add_f32_e32 v19, 1.0, v19
	v_rcp_f32_e32 v75, v19
	v_mul_f32_e32 v19, 0xbfb8aa3b, v25
	v_exp_f32_e32 v19, v19
	v_pk_mul_f32 v[22:23], v[74:75], v[22:23]
	s_nop 0
	v_mul_f32_e32 v21, v22, v23
	v_add_f32_e32 v19, 1.0, v19
	v_rcp_f32_e32 v23, v19
	v_mul_f32_e32 v19, 0xbfb8aa3b, v59
	v_exp_f32_e32 v19, v19
	v_mul_f32_e32 v22, v78, v27
	v_pk_mul_f32 v[22:23], v[22:23], v[24:25]
	v_lshlrev_b32_e32 v27, 16, v73
	v_add_f32_e32 v19, 1.0, v19
	v_mul_f32_e32 v24, v22, v23
	v_rcp_f32_e32 v23, v19
	v_mul_f32_e32 v19, 0xbfb8aa3b, v61
	v_exp_f32_e32 v19, v19
	v_mul_f32_e32 v22, v78, v28
	v_pk_mul_f32 v[22:23], v[22:23], v[58:59]
	v_mov_b32_e32 v28, v53
	v_add_f32_e32 v19, 1.0, v19
	v_mul_f32_e32 v25, v22, v23
	v_rcp_f32_e32 v23, v19
	v_mul_f32_e32 v22, v78, v29
	v_cvt_pk_fp8_f32 v19, v21, v24
	v_pk_mul_f32 v[22:23], v[22:23], v[60:61]
	v_mov_b32_e32 v24, v51
	v_mul_f32_e32 v22, v22, v23
	v_lshlrev_b32_e32 v23, 16, v72
	v_mul_f32_e32 v21, 0xbfb8aa3b, v23
	v_exp_f32_e32 v21, v21
	v_cvt_pk_fp8_f32 v19, v25, v22 op_sel:[0,0,1]
	v_and_b32_e32 v25, 0xffff0000, v72
	v_mov_b32_e32 v22, v50
	v_add_f32_e32 v21, 1.0, v21
	v_rcp_f32_e32 v55, v21
	v_mul_f32_e32 v21, 0xbfb8aa3b, v25
	v_exp_f32_e32 v21, v21
	v_and_b32_e32 v29, 0xffff0000, v73
	v_pk_mul_f32 v[22:23], v[54:55], v[22:23]
	v_permlane32_swap_b32_e32 v18, v19
	v_add_f32_e32 v21, 1.0, v21
	v_mul_f32_e32 v30, v22, v23
	v_rcp_f32_e32 v23, v21
	v_mul_f32_e32 v21, 0xbfb8aa3b, v27
	v_exp_f32_e32 v21, v21
	v_mul_f32_e32 v22, v78, v31
	v_pk_mul_f32 v[22:23], v[22:23], v[24:25]
	v_add_f32_e32 v21, 1.0, v21
	v_mul_f32_e32 v24, v22, v23
	v_rcp_f32_e32 v23, v21
	v_mul_f32_e32 v21, 0xbfb8aa3b, v29
	v_exp_f32_e32 v21, v21
	v_mul_f32_e32 v22, v78, v32
	v_pk_mul_f32 v[22:23], v[22:23], v[26:27]
	v_mul_f32_e32 v26, v78, v2
	v_add_f32_e32 v21, 1.0, v21
	v_mul_f32_e32 v25, v22, v23
	v_rcp_f32_e32 v23, v21
	v_cvt_pk_fp8_f32 v21, v30, v24
	v_mul_f32_e32 v22, v78, v33
	v_pk_mul_f32 v[22:23], v[22:23], v[28:29]
	s_waitcnt vmcnt(3)
	v_mov_b32_e32 v24, v49
	v_mul_f32_e32 v22, v22, v23
	v_cvt_pk_fp8_f32 v21, v25, v22 op_sel:[0,0,1]
	v_lshlrev_b32_e32 v23, 16, v71
	v_mov_b32_e32 v22, v48
	v_and_b32_e32 v25, 0xffff0000, v71
	v_permlane32_swap_b32_e32 v20, v21
	global_store_dwordx4 v[62:63], v[18:21], off offset:768
	s_nop 1
	v_lshlrev_b32_e32 v19, 16, v70
	v_mul_f32_e32 v18, 0xbfb8aa3b, v19
	v_exp_f32_e32 v18, v18
	v_and_b32_e32 v21, 0xffff0000, v70
	v_mul_f32_e32 v2, 0xbfb8aa3b, v21
	v_exp_f32_e32 v2, v2
	v_add_f32_e32 v18, 1.0, v18
	v_rcp_f32_e32 v27, v18
	v_mov_b32_e32 v18, v46
	v_add_f32_e32 v2, 1.0, v2
	v_mov_b32_e32 v20, v47
	v_pk_mul_f32 v[18:19], v[26:27], v[18:19]
	s_nop 0
	v_mul_f32_e32 v26, v18, v19
	v_rcp_f32_e32 v19, v2
	v_mul_f32_e32 v18, v78, v3
	v_pk_mul_f32 v[2:3], v[18:19], v[20:21]
	s_nop 0
	v_mul_f32_e32 v18, v2, v3
	v_mul_f32_e32 v2, 0xbfb8aa3b, v23
	v_exp_f32_e32 v2, v2
	v_and_b32_e32 v19, 0xffff0000, v68
	v_lshlrev_b32_e32 v21, 16, v69
	s_waitcnt vmcnt(3)
	v_mov_b32_e32 v20, v44
	v_add_f32_e32 v2, 1.0, v2
	v_rcp_f32_e32 v3, v2
	v_mul_f32_e32 v2, v78, v4
	v_pk_mul_f32 v[2:3], v[2:3], v[22:23]
	s_nop 0
	v_mul_f32_e32 v4, v2, v3
	v_mul_f32_e32 v2, 0xbfb8aa3b, v25
	v_exp_f32_e32 v2, v2
	v_and_b32_e32 v23, 0xffff0000, v69
	v_mov_b32_e32 v22, v45
	v_add_f32_e32 v2, 1.0, v2
	v_rcp_f32_e32 v3, v2
	v_mul_f32_e32 v2, v78, v5
	v_lshlrev_b32_e32 v5, 16, v68
	v_pk_mul_f32 v[2:3], v[2:3], v[24:25]
	s_nop 0
	v_mul_f32_e32 v3, v2, v3
	v_cvt_pk_fp8_f32 v2, v26, v18
	v_mul_f32_e32 v24, v78, v6
	v_mov_b32_e32 v18, v43
	v_cvt_pk_fp8_f32 v2, v4, v3 op_sel:[0,0,1]
	v_mul_f32_e32 v3, 0xbfb8aa3b, v5
	v_exp_f32_e32 v3, v3
	v_mov_b32_e32 v4, v42
	v_add_f32_e32 v3, 1.0, v3
	v_rcp_f32_e32 v25, v3
	s_nop 0
	v_pk_mul_f32 v[4:5], v[24:25], v[4:5]
	s_nop 0
	v_mul_f32_e32 v3, v4, v5
	v_mul_f32_e32 v4, 0xbfb8aa3b, v19
	v_exp_f32_e32 v4, v4
	s_nop 0
	v_add_f32_e32 v4, 1.0, v4
	v_rcp_f32_e32 v5, v4
	v_mul_f32_e32 v4, v78, v7
	v_pk_mul_f32 v[4:5], v[4:5], v[18:19]
	s_nop 0
	v_mul_f32_e32 v6, v4, v5
	v_mul_f32_e32 v4, 0xbfb8aa3b, v21
	v_exp_f32_e32 v4, v4
	v_lshlrev_b32_e32 v19, 16, v67
	s_waitcnt vmcnt(2)
	v_mov_b32_e32 v18, v40
	v_add_f32_e32 v4, 1.0, v4
	v_rcp_f32_e32 v5, v4
	v_mul_f32_e32 v4, v78, v8
	v_mov_b32_e32 v8, v39
	v_pk_mul_f32 v[4:5], v[4:5], v[20:21]
	s_nop 0
	v_mul_f32_e32 v7, v4, v5
	v_mul_f32_e32 v4, 0xbfb8aa3b, v23
	v_exp_f32_e32 v4, v4
	v_and_b32_e32 v21, 0xffff0000, v67
	v_mov_b32_e32 v20, v41
	v_add_f32_e32 v4, 1.0, v4
	v_rcp_f32_e32 v5, v4
	v_mul_f32_e32 v4, v78, v9
	v_and_b32_e32 v9, 0xffff0000, v66
	v_pk_mul_f32 v[4:5], v[4:5], v[22:23]
	s_nop 0
	v_mul_f32_e32 v5, v4, v5
	v_cvt_pk_fp8_f32 v4, v3, v6
	v_mul_f32_e32 v22, v78, v10
	v_mov_b32_e32 v6, v38
	s_waitcnt vmcnt(1)
	v_mov_b32_e32 v10, v36
	v_cvt_pk_fp8_f32 v4, v7, v5 op_sel:[0,0,1]
	v_lshlrev_b32_e32 v7, 16, v66
	v_mul_f32_e32 v3, 0xbfb8aa3b, v7
	v_exp_f32_e32 v3, v3
	s_nop 0
	v_add_f32_e32 v3, 1.0, v3
	v_rcp_f32_e32 v23, v3
	v_mul_f32_e32 v3, 0xbfb8aa3b, v9
	v_exp_f32_e32 v3, v3
	v_pk_mul_f32 v[6:7], v[22:23], v[6:7]
	s_nop 0
	v_mul_f32_e32 v5, v6, v7
	v_add_f32_e32 v3, 1.0, v3
	v_rcp_f32_e32 v7, v3
	v_mul_f32_e32 v3, 0xbfb8aa3b, v19
	v_exp_f32_e32 v3, v3
	v_mul_f32_e32 v6, v78, v11
	v_pk_mul_f32 v[6:7], v[6:7], v[8:9]
	v_lshlrev_b32_e32 v11, 16, v65
	v_add_f32_e32 v3, 1.0, v3
	v_mul_f32_e32 v8, v6, v7
	v_rcp_f32_e32 v7, v3
	v_mul_f32_e32 v3, 0xbfb8aa3b, v21
	v_exp_f32_e32 v3, v3
	v_mul_f32_e32 v6, v78, v12
	v_pk_mul_f32 v[6:7], v[6:7], v[18:19]
	v_mul_f32_e32 v18, v78, v14
	v_add_f32_e32 v3, 1.0, v3
	v_mul_f32_e32 v9, v6, v7
	v_rcp_f32_e32 v7, v3
	v_mul_f32_e32 v6, v78, v13
	v_cvt_pk_fp8_f32 v3, v5, v8
	v_pk_mul_f32 v[6:7], v[6:7], v[20:21]
	v_mov_b32_e32 v8, v35
	v_mul_f32_e32 v6, v6, v7
	v_lshlrev_b32_e32 v7, 16, v64
	v_mul_f32_e32 v5, 0xbfb8aa3b, v7
	v_exp_f32_e32 v5, v5
	v_cvt_pk_fp8_f32 v3, v9, v6 op_sel:[0,0,1]
	v_and_b32_e32 v9, 0xffff0000, v64
	v_mov_b32_e32 v6, v34
	v_add_f32_e32 v5, 1.0, v5
	v_rcp_f32_e32 v19, v5
	v_mul_f32_e32 v5, 0xbfb8aa3b, v9
	v_exp_f32_e32 v5, v5
	v_and_b32_e32 v13, 0xffff0000, v65
	v_pk_mul_f32 v[6:7], v[18:19], v[6:7]
	v_mov_b32_e32 v12, v37
	v_add_f32_e32 v5, 1.0, v5
	v_mul_f32_e32 v14, v6, v7
	v_rcp_f32_e32 v7, v5
	v_mul_f32_e32 v5, 0xbfb8aa3b, v11
	v_exp_f32_e32 v5, v5
	v_mul_f32_e32 v6, v78, v15
	v_pk_mul_f32 v[6:7], v[6:7], v[8:9]
	v_permlane32_swap_b32_e32 v2, v3
	v_add_f32_e32 v5, 1.0, v5
	v_mul_f32_e32 v8, v6, v7
	v_rcp_f32_e32 v7, v5
	v_mul_f32_e32 v5, 0xbfb8aa3b, v13
	v_exp_f32_e32 v5, v5
	v_mul_f32_e32 v6, v78, v16
	v_pk_mul_f32 v[6:7], v[6:7], v[10:11]
	v_add_f32_e32 v5, 1.0, v5
	v_mul_f32_e32 v9, v6, v7
	v_rcp_f32_e32 v7, v5
	v_cvt_pk_fp8_f32 v5, v14, v8
	v_mul_f32_e32 v6, v78, v17
	v_pk_mul_f32 v[6:7], v[6:7], v[12:13]
	s_nop 0
	v_mul_f32_e32 v6, v6, v7
	v_cvt_pk_fp8_f32 v5, v9, v6 op_sel:[0,0,1]
	s_nop 1
	v_permlane32_swap_b32_e32 v4, v5
	global_store_dwordx4 v[62:63], v[2:5], off offset:800
	s_cbranch_vccz .LBB0_550
	s_waitcnt vmcnt(0)
	s_barrier
	s_and_saveexec_b64 s[4:5], s[0:1]
	s_cbranch_execz .LBB0_549
	s_mov_b64 s[10:11], exec
	v_mbcnt_lo_u32_b32 v2, s10, 0
	buffer_wbl2 sc1
	s_waitcnt vmcnt(0)
	s_waitcnt vmcnt(0)
	v_mbcnt_hi_u32_b32 v2, s11, v2
	v_cmp_eq_u32_e32 vcc, 0, v2
	s_and_b64 s[14:15], exec, vcc
	s_mov_b64 exec, s[14:15]
	s_cbranch_execz .LBB0_549
	s_bcnt1_i32_b64 s10, s[10:11]
	v_mov_b32_e32 v2, s10
	global_atomic_add v0, v2, s[84:85]
	s_branch .LBB0_549
